# baseline (speedup 1.0000x reference)
_Z14combine_kernelPKDF16_PK15HIP_vector_typeIfLj2EEPDF16_:
	s_load_dwordx4 s[4:7], s[0:1], 0x0
	s_load_dwordx2 s[8:9], s[0:1], 0x10
	v_lshl_or_b32 v0, s2, 8, v0
	s_mov_b32 s0, 0x2aaaaaab
	v_mul_hi_i32 v1, v0, s0
	v_lshrrev_b32_e32 v2, 31, v1
	v_ashrrev_i32_e32 v1, 3, v1
	v_add_u32_e32 v10, v1, v2
	s_movk_i32 s0, 0xffd0
	v_mad_u64_u32 v[2:3], s[0:1], v10, s0, v[0:1]
	v_ashrrev_i32_e32 v1, 31, v0
	v_lshlrev_b64 v[16:17], 5, v[0:1]
	v_ashrrev_i32_e32 v11, 2, v2
	v_ashrrev_i32_e32 v12, 11, v10
	s_waitcnt lgkmcnt(0)
	v_lshl_add_u64 v[8:9], s[4:5], 0, v[16:17]
	s_mov_b64 s[0:1], 0x600000
	v_and_b32_e32 v24, 0x7ff, v10
	v_mad_i32_i24 v10, v12, 12, v11
	v_lshl_add_u64 v[20:21], v[8:9], 0, s[0:1]
	s_mov_b32 s0, 0x600000
	v_ashrrev_i32_e32 v11, 31, v10
	v_add_co_u32_e32 v22, vcc, s0, v8
	v_lshlrev_b64 v[18:19], 14, v[10:11]
	s_nop 0
	v_addc_co_u32_e32 v23, vcc, 0, v9, vcc
	global_load_dwordx4 v[0:3], v[8:9], off nt
	global_load_dwordx4 v[4:7], v[8:9], off offset:16 nt
	s_nop 0
	global_load_dwordx4 v[8:11], v[22:23], off nt
	global_load_dwordx4 v[12:15], v[20:21], off offset:16 nt
	v_lshl_add_u64 v[18:19], s[6:7], 0, v[18:19]
	v_lshlrev_b32_e32 v20, 3, v24
	v_mov_b32_e32 v21, 0
	v_lshl_add_u64 v[18:19], v[18:19], 0, v[20:21]
	s_mov_b32 s0, 0x60000
	v_add_co_u32_e32 v20, vcc, s0, v18
	s_nop 1
	v_addc_co_u32_e32 v21, vcc, 0, v19, vcc
	global_load_dwordx2 v[22:23], v[18:19], off
	global_load_dwordx2 v[24:25], v[20:21], off
	s_waitcnt vmcnt(5)
	v_cvt_f32_f16_e32 v41, v3
	s_waitcnt vmcnt(4)
	v_cvt_f32_f16_sdwa v37, v6 dst_sel:DWORD dst_unused:UNUSED_PAD src0_sel:WORD_1
	v_cvt_f32_f16_e32 v38, v6
	v_cvt_f32_f16_sdwa v43, v3 dst_sel:DWORD dst_unused:UNUSED_PAD src0_sel:WORD_1
	v_cvt_f32_f16_e32 v21, v1
	v_cvt_f32_f16_sdwa v34, v1 dst_sel:DWORD dst_unused:UNUSED_PAD src0_sel:WORD_1
	s_waitcnt vmcnt(3)
	v_cvt_f32_f16_e32 v1, v8
	v_cvt_f32_f16_sdwa v20, v8 dst_sel:DWORD dst_unused:UNUSED_PAD src0_sel:WORD_1
	v_cvt_f32_f16_e32 v27, v9
	v_cvt_f32_f16_sdwa v32, v9 dst_sel:DWORD dst_unused:UNUSED_PAD src0_sel:WORD_1
	v_cvt_f32_f16_e32 v35, v10
	v_cvt_f32_f16_sdwa v40, v10 dst_sel:DWORD dst_unused:UNUSED_PAD src0_sel:WORD_1
	v_cvt_f32_f16_sdwa v29, v5 dst_sel:DWORD dst_unused:UNUSED_PAD src0_sel:WORD_1
	v_cvt_f32_f16_e32 v30, v5
	s_waitcnt vmcnt(2)
	v_cvt_f32_f16_e32 v18, v12
	v_cvt_f32_f16_sdwa v5, v12 dst_sel:DWORD dst_unused:UNUSED_PAD src0_sel:WORD_1
	v_cvt_f32_f16_e32 v28, v13
	v_cvt_f32_f16_sdwa v31, v13 dst_sel:DWORD dst_unused:UNUSED_PAD src0_sel:WORD_1
	v_cvt_f32_f16_sdwa v42, v11 dst_sel:DWORD dst_unused:UNUSED_PAD src0_sel:WORD_1
	v_cvt_f32_f16_e32 v36, v14
	v_cvt_f32_f16_sdwa v39, v14 dst_sel:DWORD dst_unused:UNUSED_PAD src0_sel:WORD_1
	v_cvt_f32_f16_sdwa v19, v4 dst_sel:DWORD dst_unused:UNUSED_PAD src0_sel:WORD_1
	v_cvt_f32_f16_e32 v4, v4
	v_cvt_f32_f16_sdwa v26, v0 dst_sel:DWORD dst_unused:UNUSED_PAD src0_sel:WORD_1
	v_cvt_f32_f16_e32 v33, v2
	v_cvt_f32_f16_sdwa v2, v2 dst_sel:DWORD dst_unused:UNUSED_PAD src0_sel:WORD_1
	s_waitcnt vmcnt(1)
	v_max_f32_e32 v3, v22, v22
	s_waitcnt vmcnt(0)
	v_max_f32_e32 v6, v24, v24
	v_max_f32_e32 v3, v3, v6
	v_sub_f32_e32 v6, v22, v3
	v_sub_f32_e32 v3, v24, v3
	v_exp_f32_e32 v9, v6
	v_exp_f32_e32 v8, v3
	v_mov_b32_e32 v22, v25
	v_cvt_f32_f16_e32 v3, v11
	v_pk_mul_f32 v[8:9], v[22:23], v[8:9]
	s_nop 0
	v_add_f32_e32 v6, v9, v8
	v_div_scale_f32 v10, s[0:1], v6, v6, 1.0
	v_rcp_f32_e32 v12, v10
	v_div_scale_f32 v11, vcc, 1.0, v6, 1.0
	v_fma_f32 v13, -v10, v12, 1.0
	v_fmac_f32_e32 v12, v13, v12
	v_mul_f32_e32 v13, v11, v12
	v_fma_f32 v14, -v10, v13, v11
	v_fmac_f32_e32 v13, v14, v12
	v_fma_f32 v10, -v10, v13, v11
	v_div_fmas_f32 v10, v10, v12, v13
	v_div_fixup_f32 v6, v10, v6, 1.0
	v_pk_mul_f32 v[8:9], v[8:9], v[6:7] op_sel_hi:[1,0]
	s_nop 0
	v_mul_f32_e32 v1, v8, v1
	v_pk_mul_f32 v[4:5], v[8:9], v[4:5] op_sel:[1,0] op_sel_hi:[0,1]
	v_pk_mul_f32 v[10:11], v[8:9], v[26:27] op_sel:[1,0] op_sel_hi:[0,1]
	v_pk_mul_f32 v[12:13], v[8:9], v[30:31] op_sel:[1,0] op_sel_hi:[0,1]
	v_pk_mul_f32 v[22:23], v[8:9], v[34:35] op_sel:[1,0] op_sel_hi:[0,1]
	v_pk_mul_f32 v[2:3], v[8:9], v[2:3] op_sel:[1,0] op_sel_hi:[0,1]
	v_fma_mixlo_f16 v6, v9, v0, v1 op_sel_hi:[0,1,0]
	v_pk_fma_f32 v[0:1], v[8:9], v[18:19], v[4:5]
	v_pk_fma_f32 v[4:5], v[8:9], v[20:21], v[10:11]
	v_pk_fma_f32 v[10:11], v[8:9], v[28:29], v[12:13]
	v_pk_fma_f32 v[12:13], v[8:9], v[32:33], v[22:23]
	v_pk_fma_f32 v[20:21], v[8:9], v[40:41], v[2:3]
	v_cvt_pk_f16_f32 v0, v0, v1
	v_cvt_pk_f16_f32 v3, v4, v5
	v_cvt_pk_f16_f32 v1, v10, v11
	v_cvt_pk_f16_f32 v14, v12, v13
	v_pk_mul_f32 v[10:11], v[8:9], v[42:43]
	v_cvt_f32_f16_e32 v12, v7
	v_cvt_f32_f16_sdwa v13, v15 dst_sel:DWORD dst_unused:UNUSED_PAD src0_sel:WORD_1
	v_pack_b32_f16 v4, v6, v3
	v_alignbit_b32 v5, v14, v3, 16
	v_add_f32_e32 v3, v11, v10
	v_cvt_f32_f16_sdwa v11, v7 dst_sel:DWORD dst_unused:UNUSED_PAD src0_sel:WORD_1
	v_cvt_f32_f16_e32 v10, v15
	v_cvt_f16_f32_e32 v3, v3
	v_pk_mul_f32 v[24:25], v[8:9], v[38:39] op_sel:[1,0] op_sel_hi:[0,1]
	v_pk_fma_f32 v[18:19], v[8:9], v[36:37], v[24:25]
	v_pk_mul_f32 v[12:13], v[8:9], v[12:13] op_sel:[1,0] op_sel_hi:[0,1]
	v_cvt_pk_f16_f32 v2, v18, v19
	v_cvt_pk_f16_f32 v18, v20, v21
	v_pk_fma_f32 v[8:9], v[8:9], v[10:11], v[12:13]
	v_alignbit_b32 v6, v18, v14, 16
	v_alignbit_b32 v7, v3, v18, 16
	v_cvt_pk_f16_f32 v3, v8, v9
	v_lshl_add_u64 v[8:9], s[8:9], 0, v[16:17]
	global_store_dwordx4 v[8:9], v[4:7], off
	global_store_dwordx4 v[8:9], v[0:3], off offset:16
	s_endpgm
